# stream: XCD-contiguous 16MB regions (chunk = (blk>>3) + (blk&7)*32) plus rotated wave-row assignment
# baseline (speedup 1.0000x reference)
_Z13stream_kernelPKfPf:
	s_mov_b32 s11, s2
	s_lshr_b32 s10, s2, 3
	s_and_b32 s2, s2, 7
	s_lshl_b32 s2, s2, 5
	s_or_b32 s2, s2, s10
	s_load_dwordx4 s[4:7], s[0:1], 0x0
	s_movk_i32 s0, 0x100
	v_readfirstlane_b32 s3, v0
	v_cmp_gt_u32_e32 vcc, s0, v0
	s_and_saveexec_b64 s[0:1], vcc
	s_cbranch_execz .LBB1_2
	v_lshlrev_b32_e32 v18, 4, v0
	v_mov_b32_e32 v19, 0
	s_waitcnt lgkmcnt(0)
	v_lshl_add_u64 v[14:15], s[6:7], 0, v[18:19]
	v_add_co_u32_e32 v16, vcc, 0x1000, v14
	global_load_dwordx4 v[2:5], v18, s[6:7]
	s_nop 0
	v_addc_co_u32_e32 v17, vcc, 0, v15, vcc
	v_add_co_u32_e32 v20, vcc, 0x2000, v14
	s_nop 1
	v_addc_co_u32_e32 v21, vcc, 0, v15, vcc
	v_add_co_u32_e32 v14, vcc, 0x3000, v14
	global_load_dwordx4 v[6:9], v[16:17], off
	global_load_dwordx4 v[10:13], v[20:21], off
	v_addc_co_u32_e32 v15, vcc, 0, v15, vcc
	global_load_dwordx4 v[14:17], v[14:15], off
	s_waitcnt vmcnt(2)
	v_pk_add_f32 v[4:5], v[4:5], v[8:9]
	v_pk_add_f32 v[2:3], v[2:3], v[6:7]
	s_waitcnt vmcnt(1)
	v_pk_add_f32 v[4:5], v[4:5], v[12:13]
	v_pk_add_f32 v[2:3], v[2:3], v[10:11]
	s_waitcnt vmcnt(0)
	v_pk_add_f32 v[4:5], v[4:5], v[16:17]
	v_pk_add_f32 v[2:3], v[2:3], v[14:15]
	ds_write_b128 v18, v[2:5]
.LBB1_2:
	s_or_b64 exec, exec, s[0:1]
	s_lshr_b32 s8, s3, 6
	s_add_i32 s8, s8, s11
	s_and_b32 s8, s8, 15
	s_lshl_b32 s0, s2, 7
	v_and_b32_e32 v24, 63, v0
	s_add_i32 s9, s8, s0
	s_waitcnt lgkmcnt(0)
	s_and_b32 s1, s5, 0xffff
	s_mov_b32 s3, 0x20000
	s_brev_b32 s2, 16
	s_mov_b32 s0, s4
	v_lshlrev_b32_e32 v25, 4, v24
	s_lshl_b32 s4, s9, 12
	buffer_load_dwordx4 v[26:29], v25, s[0:3], s4 offen offset:1024 nt
	buffer_load_dwordx4 v[30:33], v25, s[0:3], s4 offen nt
	buffer_load_dwordx4 v[34:37], v25, s[0:3], s4 offen offset:2048 nt
	s_add_i32 s5, s4, 0x10000
	buffer_load_dwordx4 v[38:41], v25, s[0:3], s5 offen offset:1024 nt
	buffer_load_dwordx4 v[42:45], v25, s[0:3], s5 offen nt
	buffer_load_dwordx4 v[16:19], v25, s[0:3], s4 offen offset:3072 nt
	s_add_i32 s10, s4, 0x20000
	buffer_load_dwordx4 v[46:49], v25, s[0:3], s5 offen offset:2048 nt
	buffer_load_dwordx4 v[20:23], v25, s[0:3], s5 offen offset:3072 nt
	s_barrier
	buffer_load_dwordx4 v[50:53], v25, s[0:3], s10 offen offset:1024 nt
	buffer_load_dwordx4 v[54:57], v25, s[0:3], s10 offen nt
	ds_read_b128 v[4:7], v25 offset:1024
	ds_read_b128 v[0:3], v25
	ds_read_b128 v[12:15], v25 offset:2048
	ds_read_b128 v[8:11], v25 offset:3072
	s_add_i32 s5, s4, 0x30000
	v_cmp_gt_u32_e32 vcc, 8, v24
	s_waitcnt vmcnt(9) lgkmcnt(3)
	v_pk_mul_f32 v[28:29], v[6:7], v[28:29]
	v_pk_mul_f32 v[26:27], v[4:5], v[26:27]
	s_waitcnt vmcnt(8) lgkmcnt(2)
	v_pk_fma_f32 v[32:33], v[2:3], v[32:33], v[28:29]
	v_pk_fma_f32 v[30:31], v[0:1], v[30:31], v[26:27]
	buffer_load_dwordx4 v[26:29], v25, s[0:3], s5 offen offset:1024 nt
	s_waitcnt vmcnt(8) lgkmcnt(1)
	v_pk_fma_f32 v[58:59], v[14:15], v[36:37], v[32:33]
	v_pk_fma_f32 v[60:61], v[12:13], v[34:35], v[30:31]
	buffer_load_dwordx4 v[30:33], v25, s[0:3], s5 offen nt
	s_waitcnt vmcnt(8)
	v_pk_mul_f32 v[34:35], v[6:7], v[40:41]
	v_pk_mul_f32 v[36:37], v[4:5], v[38:39]
	s_waitcnt vmcnt(7)
	v_pk_fma_f32 v[44:45], v[2:3], v[44:45], v[34:35]
	v_pk_fma_f32 v[42:43], v[0:1], v[42:43], v[36:37]
	buffer_load_dwordx4 v[34:37], v25, s[0:3], s10 offen offset:2048 nt
	s_waitcnt vmcnt(4)
	v_pk_mul_f32 v[38:39], v[6:7], v[52:53]
	v_pk_mul_f32 v[40:41], v[4:5], v[50:51]
	s_waitcnt vmcnt(3)
	v_pk_fma_f32 v[50:51], v[2:3], v[56:57], v[38:39]
	v_pk_fma_f32 v[52:53], v[0:1], v[54:55], v[40:41]
	buffer_load_dwordx4 v[38:41], v25, s[0:3], s10 offen offset:3072 nt
	v_pk_fma_f32 v[48:49], v[14:15], v[48:49], v[44:45]
	v_pk_fma_f32 v[46:47], v[12:13], v[46:47], v[42:43]
	s_waitcnt lgkmcnt(0)
	v_pk_fma_f32 v[18:19], v[10:11], v[18:19], v[58:59]
	v_pk_fma_f32 v[16:17], v[8:9], v[16:17], v[60:61]
	v_add_f32_e32 v61, v18, v19
	v_add_f32_e32 v60, v16, v17
	v_pk_fma_f32 v[16:17], v[10:11], v[22:23], v[48:49]
	v_pk_fma_f32 v[18:19], v[8:9], v[20:21], v[46:47]
	v_add_f32_e32 v16, v16, v17
	v_add_f32_e32 v18, v18, v19
	v_add_f32_e32 v60, v60, v61
	v_add_f32_e32 v16, v18, v16
	s_add_i32 s10, s4, 0x50000
	s_waitcnt vmcnt(3)
	v_pk_mul_f32 v[28:29], v[6:7], v[28:29]
	v_pk_mul_f32 v[26:27], v[4:5], v[26:27]
	v_add_f32_dpp v16, v16, v16 quad_perm:[1,0,3,2] row_mask:0xf bank_mask:0xf bound_ctrl:1
	s_waitcnt vmcnt(2)
	v_pk_fma_f32 v[54:55], v[2:3], v[32:33], v[28:29]
	v_pk_fma_f32 v[56:57], v[0:1], v[30:31], v[26:27]
	buffer_load_dwordx4 v[26:29], v25, s[0:3], s5 offen offset:2048 nt
	buffer_load_dwordx4 v[30:33], v25, s[0:3], s5 offen offset:3072 nt
	s_add_i32 s5, s4, 0x40000
	buffer_load_dwordx4 v[42:45], v25, s[0:3], s5 offen offset:1024 nt
	s_waitcnt vmcnt(4)
	v_pk_fma_f32 v[50:51], v[14:15], v[36:37], v[50:51]
	v_pk_fma_f32 v[52:53], v[12:13], v[34:35], v[52:53]
	buffer_load_dwordx4 v[34:37], v25, s[0:3], s5 offen nt
	v_add_f32_dpp v16, v16, v16 quad_perm:[2,3,0,1] row_mask:0xf bank_mask:0xf bound_ctrl:1
	s_waitcnt vmcnt(4)
	v_pk_fma_f32 v[58:59], v[10:11], v[40:41], v[50:51]
	v_pk_fma_f32 v[38:39], v[8:9], v[38:39], v[52:53]
	v_add_f32_e32 v19, v58, v59
	v_add_f32_e32 v17, v38, v39
	v_add_f32_dpp v58, v60, v60 quad_perm:[1,0,3,2] row_mask:0xf bank_mask:0xf bound_ctrl:1
	v_add_f32_e32 v18, v17, v19
	v_add_f32_dpp v16, v16, v16 row_ror:4 row_mask:0xf bank_mask:0xf bound_ctrl:1
	v_add_f32_dpp v17, v58, v58 quad_perm:[2,3,0,1] row_mask:0xf bank_mask:0xf bound_ctrl:1
	buffer_load_dwordx4 v[20:23], v25, s[0:3], s5 offen offset:2048 nt
	buffer_load_dwordx4 v[46:49], v25, s[0:3], s5 offen offset:3072 nt
	v_add_f32_dpp v17, v17, v17 row_ror:4 row_mask:0xf bank_mask:0xf bound_ctrl:1
	v_add_f32_dpp v58, v16, v16 row_ror:8 row_mask:0xf bank_mask:0xf bound_ctrl:1
	buffer_load_dwordx4 v[38:41], v25, s[0:3], s10 offen nt
	buffer_load_dwordx4 v[50:53], v25, s[0:3], s10 offen offset:1024 nt
	v_add_f32_dpp v17, v17, v17 row_ror:8 row_mask:0xf bank_mask:0xf bound_ctrl:1
	v_mov_b32_e32 v19, v17
	v_mov_b32_e32 v59, v58
	s_nop 0
	v_permlane16_swap_b32_e32 v17, v19
	v_permlane16_swap_b32_e32 v58, v59
	v_add_f32_e32 v16, v17, v19
	v_add_f32_e32 v17, v58, v59
	s_add_i32 s5, s4, 0x60000
	s_add_i32 s4, s4, 0x70000
	v_add_f32_dpp v18, v18, v18 quad_perm:[1,0,3,2] row_mask:0xf bank_mask:0xf bound_ctrl:1
	s_waitcnt vmcnt(7)
	v_pk_fma_f32 v[28:29], v[14:15], v[28:29], v[54:55]
	v_pk_fma_f32 v[54:55], v[12:13], v[26:27], v[56:57]
	s_waitcnt vmcnt(6)
	v_pk_fma_f32 v[58:59], v[10:11], v[32:33], v[28:29]
	buffer_load_dwordx4 v[26:29], v25, s[0:3], s10 offen offset:2048 nt
	v_pk_fma_f32 v[54:55], v[8:9], v[30:31], v[54:55]
	buffer_load_dwordx4 v[30:33], v25, s[0:3], s10 offen offset:3072 nt
	v_add_f32_e32 v66, v54, v55
	s_waitcnt vmcnt(7)
	v_pk_mul_f32 v[54:55], v[6:7], v[44:45]
	v_pk_mul_f32 v[56:57], v[4:5], v[42:43]
	buffer_load_dwordx4 v[42:45], v25, s[0:3], s5 offen offset:1024 nt
	s_waitcnt vmcnt(7)
	v_pk_fma_f32 v[54:55], v[2:3], v[36:37], v[54:55]
	v_pk_fma_f32 v[56:57], v[0:1], v[34:35], v[56:57]
	buffer_load_dwordx4 v[34:37], v25, s[0:3], s5 offen nt
	v_add_f32_dpp v18, v18, v18 quad_perm:[2,3,0,1] row_mask:0xf bank_mask:0xf bound_ctrl:1
	s_waitcnt vmcnt(7)
	v_pk_fma_f32 v[22:23], v[14:15], v[22:23], v[54:55]
	v_pk_fma_f32 v[20:21], v[12:13], v[20:21], v[56:57]
	s_waitcnt vmcnt(6)
	v_pk_fma_f32 v[60:61], v[10:11], v[48:49], v[22:23]
	v_pk_fma_f32 v[22:23], v[8:9], v[46:47], v[20:21]
	s_waitcnt vmcnt(4)
	v_pk_mul_f32 v[54:55], v[4:5], v[50:51]
	v_pk_mul_f32 v[20:21], v[6:7], v[52:53]
	v_pk_fma_f32 v[38:39], v[0:1], v[38:39], v[54:55]
	buffer_load_dwordx4 v[46:49], v25, s[0:3], s5 offen offset:2048 nt
	buffer_load_dwordx4 v[50:53], v25, s[0:3], s5 offen offset:3072 nt
	v_pk_fma_f32 v[20:21], v[2:3], v[40:41], v[20:21]
	v_add_f32_e32 v23, v22, v23
	v_add_f32_dpp v18, v18, v18 row_ror:4 row_mask:0xf bank_mask:0xf bound_ctrl:1
	s_waitcnt vmcnt(5)
	v_pk_fma_f32 v[26:27], v[12:13], v[26:27], v[38:39]
	buffer_load_dwordx4 v[38:41], v25, s[0:3], s4 offen nt
	buffer_load_dwordx4 v[54:57], v25, s[0:3], s4 offen offset:1024 nt
	v_pk_fma_f32 v[20:21], v[14:15], v[28:29], v[20:21]
	s_waitcnt vmcnt(6)
	v_pk_fma_f32 v[30:31], v[8:9], v[30:31], v[26:27]
	v_pk_fma_f32 v[62:63], v[10:11], v[32:33], v[20:21]
	v_add_f32_dpp v18, v18, v18 row_ror:8 row_mask:0xf bank_mask:0xf bound_ctrl:1
	s_waitcnt vmcnt(5)
	v_pk_mul_f32 v[20:21], v[6:7], v[44:45]
	v_pk_mul_f32 v[26:27], v[4:5], v[42:43]
	buffer_load_dwordx4 v[42:45], v25, s[0:3], s4 offen offset:2048 nt
	s_waitcnt vmcnt(5)
	v_pk_fma_f32 v[64:65], v[0:1], v[34:35], v[26:27]
	buffer_load_dwordx4 v[32:35], v25, s[0:3], s4 offen offset:3072 nt
	v_add_f32_e32 v27, v60, v61
	v_add_f32_e32 v23, v23, v27
	v_pk_fma_f32 v[36:37], v[2:3], v[36:37], v[20:21]
	v_add_f32_e32 v20, v58, v59
	v_add_f32_dpp v23, v23, v23 quad_perm:[1,0,3,2] row_mask:0xf bank_mask:0xf bound_ctrl:1
	v_add_f32_e32 v20, v66, v20
	v_mov_b32_e32 v19, v18
	v_add_f32_dpp v23, v23, v23 quad_perm:[2,3,0,1] row_mask:0xf bank_mask:0xf bound_ctrl:1
	v_add_f32_dpp v20, v20, v20 quad_perm:[1,0,3,2] row_mask:0xf bank_mask:0xf bound_ctrl:1
	v_permlane16_swap_b32_e32 v18, v19
	v_add_f32_dpp v23, v23, v23 row_ror:4 row_mask:0xf bank_mask:0xf bound_ctrl:1
	v_add_f32_dpp v20, v20, v20 quad_perm:[2,3,0,1] row_mask:0xf bank_mask:0xf bound_ctrl:1
	v_add_f32_e32 v18, v18, v19
	v_add_f32_dpp v23, v23, v23 row_ror:8 row_mask:0xf bank_mask:0xf bound_ctrl:1
	v_mov_b32_e32 v27, v23
	s_nop 1
	v_permlane16_swap_b32_e32 v23, v27
	v_add_f32_e32 v28, v23, v27
	v_add_f32_e32 v23, v30, v31
	s_waitcnt vmcnt(5)
	v_pk_fma_f32 v[30:31], v[14:15], v[48:49], v[36:37]
	v_pk_fma_f32 v[36:37], v[12:13], v[46:47], v[64:65]
	s_waitcnt vmcnt(4)
	v_pk_fma_f32 v[30:31], v[10:11], v[52:53], v[30:31]
	v_pk_fma_f32 v[36:37], v[8:9], v[50:51], v[36:37]
	v_add_f32_e32 v27, v62, v63
	v_add_f32_e32 v36, v36, v37
	v_add_f32_e32 v30, v30, v31
	v_add_f32_e32 v23, v23, v27
	v_add_f32_e32 v30, v36, v30
	v_add_f32_dpp v20, v20, v20 row_ror:4 row_mask:0xf bank_mask:0xf bound_ctrl:1
	v_add_f32_dpp v23, v23, v23 quad_perm:[1,0,3,2] row_mask:0xf bank_mask:0xf bound_ctrl:1
	v_add_f32_dpp v30, v30, v30 quad_perm:[1,0,3,2] row_mask:0xf bank_mask:0xf bound_ctrl:1
	v_add_f32_dpp v20, v20, v20 row_ror:8 row_mask:0xf bank_mask:0xf bound_ctrl:1
	v_add_f32_dpp v23, v23, v23 quad_perm:[2,3,0,1] row_mask:0xf bank_mask:0xf bound_ctrl:1
	v_add_f32_dpp v30, v30, v30 quad_perm:[2,3,0,1] row_mask:0xf bank_mask:0xf bound_ctrl:1
	v_mov_b32_e32 v21, v20
	v_add_f32_dpp v23, v23, v23 row_ror:4 row_mask:0xf bank_mask:0xf bound_ctrl:1
	v_add_f32_dpp v30, v30, v30 row_ror:4 row_mask:0xf bank_mask:0xf bound_ctrl:1
	v_permlane16_swap_b32_e32 v20, v21
	v_add_f32_dpp v23, v23, v23 row_ror:8 row_mask:0xf bank_mask:0xf bound_ctrl:1
	v_add_f32_dpp v30, v30, v30 row_ror:8 row_mask:0xf bank_mask:0xf bound_ctrl:1
	v_mov_b32_e32 v27, v23
	v_mov_b32_e32 v31, v30
	s_nop 0
	v_permlane16_swap_b32_e32 v23, v27
	v_permlane16_swap_b32_e32 v30, v31
	v_add_f32_e32 v21, v20, v21
	v_add_f32_e32 v23, v23, v27
	v_add_f32_e32 v30, v30, v31
	v_mov_b32_e32 v19, v16
	v_mov_b32_e32 v20, v17
	v_mov_b32_e32 v22, v18
	v_mov_b32_e32 v26, v21
	v_mov_b32_e32 v29, v28
	v_mov_b32_e32 v27, v23
	v_mov_b32_e32 v31, v30
	v_permlane32_swap_b32_e32 v16, v19
	v_permlane32_swap_b32_e32 v17, v20
	v_permlane32_swap_b32_e32 v18, v22
	v_permlane32_swap_b32_e32 v21, v26
	v_permlane32_swap_b32_e32 v28, v29
	v_permlane32_swap_b32_e32 v23, v27
	s_waitcnt vmcnt(2)
	v_pk_mul_f32 v[6:7], v[6:7], v[56:57]
	v_pk_mul_f32 v[4:5], v[4:5], v[54:55]
	v_pk_fma_f32 v[2:3], v[2:3], v[40:41], v[6:7]
	v_pk_fma_f32 v[0:1], v[0:1], v[38:39], v[4:5]
	v_permlane32_swap_b32_e32 v30, v31
	s_waitcnt vmcnt(1)
	v_pk_fma_f32 v[2:3], v[14:15], v[44:45], v[2:3]
	v_pk_fma_f32 v[0:1], v[12:13], v[42:43], v[0:1]
	s_waitcnt vmcnt(0)
	v_pk_fma_f32 v[2:3], v[10:11], v[34:35], v[2:3]
	v_pk_fma_f32 v[0:1], v[8:9], v[32:33], v[0:1]
	s_nop 0
	v_add_f32_e32 v0, v0, v1
	v_add_f32_e32 v1, v2, v3
	v_add_f32_e32 v0, v0, v1
	s_nop 1
	v_add_f32_dpp v0, v0, v0 quad_perm:[1,0,3,2] row_mask:0xf bank_mask:0xf bound_ctrl:1
	s_nop 1
	v_add_f32_dpp v0, v0, v0 quad_perm:[2,3,0,1] row_mask:0xf bank_mask:0xf bound_ctrl:1
	s_nop 1
	v_add_f32_dpp v0, v0, v0 row_ror:4 row_mask:0xf bank_mask:0xf bound_ctrl:1
	s_nop 1
	v_add_f32_dpp v0, v0, v0 row_ror:8 row_mask:0xf bank_mask:0xf bound_ctrl:1
	v_mov_b32_e32 v1, v0
	s_nop 1
	v_permlane16_swap_b32_e32 v0, v1
	v_add_f32_e32 v0, v0, v1
	v_mov_b32_e32 v1, v0
	s_nop 1
	v_permlane32_swap_b32_e32 v0, v1
	s_and_saveexec_b64 s[0:1], vcc
	s_cbranch_execz .LBB1_4
	v_add_f32_e32 v6, v16, v19
	v_cmp_eq_u32_e32 vcc, 0, v24
	v_add_f32_e32 v5, v17, v20
	v_add_f32_e32 v4, v18, v22
	v_cndmask_b32_e32 v6, 0, v6, vcc
	v_cmp_eq_u32_e32 vcc, 1, v24
	v_add_f32_e32 v3, v21, v26
	v_add_f32_e32 v2, v28, v29
	v_cndmask_b32_e32 v5, v6, v5, vcc
	v_cmp_eq_u32_e32 vcc, 2, v24
	v_add_f32_e32 v0, v0, v1
	v_add_f32_e32 v1, v30, v31
	v_cndmask_b32_e32 v4, v5, v4, vcc
	v_cmp_eq_u32_e32 vcc, 3, v24
	s_lshl_b32 s0, s8, 13
	s_and_b32 s0, s0, 0x1e000
	v_cndmask_b32_e32 v3, v4, v3, vcc
	v_cmp_eq_u32_e32 vcc, 4, v24
	s_add_u32 s0, s6, s0
	s_addc_u32 s1, s7, 0
	v_cndmask_b32_e32 v2, v3, v2, vcc
	v_add_f32_e32 v3, v23, v27
	v_cmp_eq_u32_e32 vcc, 5, v24
	s_nop 1
	v_cndmask_b32_e32 v2, v2, v3, vcc
	v_cmp_eq_u32_e32 vcc, 6, v24
	s_nop 1
	v_cndmask_b32_e32 v1, v2, v1, vcc
	v_cmp_eq_u32_e32 vcc, 7, v24
	s_nop 1
	v_cndmask_b32_e32 v2, v1, v0, vcc
	v_add_u32_e32 v0, s9, v25
	v_ashrrev_i32_e32 v0, 4, v0
	v_ashrrev_i32_e32 v1, 31, v0
	v_lshl_add_u64 v[0:1], v[0:1], 2, s[0:1]
	v_add_co_u32_e32 v0, vcc, 0x6000, v0
	s_nop 1
	v_addc_co_u32_e32 v1, vcc, 0, v1, vcc
	global_store_dword v[0:1], v2, off offset:64
